# rwkv pre-phase token loop: 59 bf16-half selects (v_and + v_lshlrev + v_cndmask on the lane-parity mask) replaced by one v_perm_b32 with a per-lane byte selector; removed slots kept as s_nop 0
# baseline (speedup 1.0000x reference)
; __device__ __forceinline__ void rwkv_pre_phase(LAS unsigned char* lds, const RwScan& a_, unsigned char* img, const int vcu, const int G, const int tid0_, const bool do_cv, const bool do_work) {
;     ...
;             int ln = tid0_ & 63; asm volatile("" : "+v"(ln));
;             const int lane = ln, fr = lane & 15, fq = lane >> 4;
;             const int h = id >> 1, t0 = tbase + 32 * (id & 1), c = h * 64 + lane;
;             const float mix_r = a_mix[c], mix_k = a_mix[1024 + c], mix_v = a_mix[2048 + c];
;             const float w0c = a_w0[c], a0c = a_a0[c], v0c = a_layer ? a_v0[c] : 0.f, kkc = a_kk[c], kac = a_ka[c], rkc = a_rk[c];
;             unsigned char* ug = img + (size_t)((b * RW_H + h) * (SEQ / 32) + (t0 >> 5)) * IMG_UNIT;
;             float cum = 0.f, er = 1.f;
;             const bool hasv = a_layer != 0;
;             unsigned prA[5], pkA[5], pvA[5], pwA[4], paA[4], pvpA[4], prB[5], pkB[5], pvB[5], pwB[4], paB[4], pvpB[4]; float pvfA[4], pvfB[4];
;             const unsigned vo2 = (unsigned)lane * 2u, vo4 = (unsigned)lane * 4u, vo2d = (unsigned)(lane >> 1) * 4u; const bool odd_lane = (lane & 1) != 0;
;             const unsigned so_proj = (unsigned)((b * SEQ + t0) * PROJ_BLD + h * 64) * 2u, so_tok = (unsigned)((b * SEQ + t0) * 1024 + h * 64);
;             const unsigned so_img = (unsigned)((b * RW_H + h) * (SEQ / 32) + (t0 >> 5)) * (unsigned)IMG_UNIT + IMG_VI;
.LBB0_412:
	s_bfe_u32 s3, s79, 0x10005
	s_lshl_b32 s9, s3, 5
	s_add_i32 s14, s72, s9
	s_lshr_b32 s14, s14, 5
	s_mul_i32 s8, s8, 0x1c4000
	v_and_b32_e32 v67, 1, v65
	v_lshlrev_b32_e32 v62, 1, v65
	s_mulk_i32 s14, 0x7100
	s_lshl_b32 s3, s3, 16
	s_add_i32 s9, s78, s9
	s_add_i32 s85, s76, s8
	s_mov_b32 s2, 0
	v_cmp_eq_u32_e64 s[6:7], 0, v67
	v_mov_b32_e32 v220, 0x03020c0c
	v_mov_b32_e32 v221, 0x01000c0c
	s_nop 1
	v_cndmask_b32_e64 v220, v220, v221, s[6:7]
	s_add_i32 s3, s77, s3
	s_mul_i32 s33, s9, 0x3000
	s_lshl_b32 s84, s9, 11
	s_add_i32 s85, s85, s14
	v_add_u32_e32 v43, s68, v62
	v_mov_b32_e32 v20, 1.0
	v_mov_b32_e32 v44, 0

.LBB0_421:
	s_waitcnt vmcnt(36)
	s_nop 0
	s_nop 0
	v_perm_b32 v15, v7, v7, v220
	s_waitcnt vmcnt(20)
	s_nop 0
	s_nop 0
	v_perm_b32 v17, v18, v18, v220
	v_sub_f32_e32 v17, v17, v15
	v_fma_f32 v18, v24, v17, v15
	s_and_b64 vcc, exec, s[90:91]
	v_mov_b32_e32 v82, v18
	s_cbranch_vccz .LBB0_423
	s_nop 0
	s_nop 0
	v_perm_b32 v17, v32, v32, v220
	v_add_f32_e32 v17, v27, v17
	v_mul_f32_e32 v17, 0xbfb8aa3b, v17
	v_exp_f32_e32 v17, v17
	s_nop 0
	s_nop 0
	v_perm_b32 v21, v35, v35, v220
	v_add_f32_e32 v17, 1.0, v17
	v_rcp_f32_e32 v17, v17
	v_sub_f32_e32 v21, v21, v18
	v_fma_f32 v82, v17, v21, v18
.LBB0_423:
	s_nop 0
	s_nop 0
	v_perm_b32 v17, v1, v1, v220
	s_nop 0
	s_nop 0
	v_perm_b32 v21, v14, v14, v220
	s_nop 0
	s_nop 0
	v_perm_b32 v14, v5, v5, v220
	s_nop 0
	s_nop 0
	v_perm_b32 v16, v16, v16, v220
	v_sub_f32_e32 v21, v21, v17
	v_sub_f32_e32 v16, v16, v14
	v_fma_f32 v85, v22, v21, v17
	v_fma_f32 v83, v23, v16, v14
	s_nop 0
	s_nop 0
	v_perm_b32 v16, v33, v33, v220
	s_nop 0
	s_nop 0
	v_perm_b32 v21, v34, v34, v220
	v_add_f32_e32 v21, v26, v21
	v_mul_f32_e32 v21, 0xbfb8aa3b, v21
	v_exp_f32_e32 v21, v21
	v_mul_f32_e32 v84, v28, v83
	v_mov_b32_e32 v88, 0
	v_mov_b32_e32 v89, 0
	v_add_f32_e32 v21, 1.0, v21
	v_rcp_f32_e32 v86, v21
	v_add_f32_e32 v16, v25, v16
	v_mul_f32_e32 v16, 0xbfb8aa3b, v16
	v_exp_f32_e32 v16, v16
	v_add_f32_e32 v21, -1.0, v86
	v_fma_f32 v87, v29, v21, 1.0
	v_mul_f32_e32 v87, v87, v83
	v_mul_f32_e32 v83, v85, v87
	v_mul_f32_e32 v21, v84, v84
	v_mul_f32_e32 v83, v30, v83
	s_nop 0
	v_permlane32_swap_b32_e32 v21, v88
	v_permlane32_swap_b32_e32 v83, v89
	v_add_f32_e32 v88, v21, v88
	v_add_f32_e32 v83, v83, v89
	s_nop 1
	v_permlane16_swap_b32_e32 v88, v83
	v_add_f32_e32 v83, v88, v83
	v_add_f32_e32 v16, 1.0, v16
	v_rcp_f32_e32 v16, v16
	v_add_f32_dpp v83, v83, v83 row_ror:8 row_mask:0xf bank_mask:0xf bound_ctrl:1
	s_add_i32 s92, s85, s2
	s_mov_b32 s14, s26
	v_add_f32_dpp v83, v83, v83 row_ror:4 row_mask:0xf bank_mask:0xf bound_ctrl:1
	v_fmac_f32_e32 v44, 0xbf60028a, v16
	v_exp_f32_e32 v21, v44
	v_add_f32_dpp v83, v83, v83 row_ror:2 row_mask:0xf bank_mask:0xf bound_ctrl:1
	v_exp_f32_e64 v16, -v44
	s_mov_b32 s15, s27
	v_add_f32_dpp v83, v83, v83 row_ror:1 row_mask:0xf bank_mask:0xf bound_ctrl:1
	s_mov_b32 s22, s26
	v_readlane_b32 s8, v83, 0
	v_readlane_b32 s9, v83, 16
	s_mov_b32 s23, s27
	v_max_f32_e64 v83, s8, s8
	v_max_f32_e32 v83, 0x179abe15, v83
	v_rsq_f32_e32 v83, v83
	s_add_i32 s8, s92, 0x4000
	s_andn2_b64 vcc, exec, s[34:35]
	v_mul_f32_e32 v83, v84, v83
	v_xor_b32_e32 v84, 0x80000000, v83
	v_pk_mul_f32 v[84:85], v[20:21], v[84:85]
	v_mul_f32_e32 v86, v86, v83
	v_mul_f32_e32 v83, s9, v82
	v_pk_mul_f32 v[86:87], v[16:17], v[86:87] op_sel_hi:[0,1]
	v_cvt_pk_bf16_f32 v16, v84, v85
	v_cvt_pk_bf16_f32 v82, v82, v83
	v_cvt_pk_bf16_f32 v20, v86, v87
	ds_write_b16 v43, v16
	ds_write_b16_d16_hi v43, v16 offset:4608
	ds_write_b16 v43, v20 offset:9216
	ds_write_b16_d16_hi v43, v20 offset:13824
	buffer_store_short v82, v62, s[12:15], s8 offen
	v_lshrrev_b32_e32 v16, 16, v82
	s_add_i32 s14, s83, s84
	buffer_store_short v16, v62, s[20:23], s14 offen
	v_cndmask_b32_e64 v16, 0, 1, s[34:35]
	v_cmp_ne_u32_e64 s[8:9], 1, v16
	s_cbranch_vccnz .LBB0_425
	v_cvt_pk_bf16_f32 v16, v18, s0
	s_mov_b32 s18, s26
	s_mov_b32 s19, s27
	buffer_store_short v16, v62, s[16:19], s14 offen
.LBB0_425:
	s_nop 0
	s_nop 0
	v_perm_b32 v20, v6, v6, v220
	v_sub_f32_e32 v15, v15, v20
	v_fma_f32 v82, v24, v15, v20
	s_and_b64 vcc, exec, s[4:5]
	v_mov_b32_e32 v83, v82
	s_cbranch_vccnz .LBB0_427
	s_nop 0
	s_nop 0
	v_perm_b32 v15, v36, v36, v220
	v_add_f32_e32 v15, v27, v15
	v_mul_f32_e32 v15, 0xbfb8aa3b, v15
	v_exp_f32_e32 v15, v15
	s_nop 0
	s_nop 0
	v_perm_b32 v16, v39, v39, v220
	v_add_f32_e32 v15, 1.0, v15
	v_rcp_f32_e32 v15, v15
	v_sub_f32_e32 v16, v16, v82
	v_fma_f32 v83, v15, v16, v82
.LBB0_427:
	s_nop 0
	s_nop 0
	v_perm_b32 v16, v2, v2, v220
	s_nop 0
	s_nop 0
	v_perm_b32 v18, v4, v4, v220
	v_sub_f32_e32 v15, v17, v16
	v_fma_f32 v85, v22, v15, v16
	s_nop 0
	s_nop 0
	v_perm_b32 v15, v37, v37, v220
	s_nop 0
	s_nop 0
	v_perm_b32 v17, v38, v38, v220
	v_add_f32_e32 v17, v26, v17
	v_mul_f32_e32 v17, 0xbfb8aa3b, v17
	v_exp_f32_e32 v17, v17
	v_add_f32_e32 v15, v25, v15
	v_mul_f32_e32 v15, 0xbfb8aa3b, v15
	v_exp_f32_e32 v15, v15
	v_add_f32_e32 v17, 1.0, v17
	v_rcp_f32_e32 v17, v17
	v_sub_f32_e32 v14, v14, v18
	v_fma_f32 v14, v23, v14, v18
	v_add_f32_e32 v15, 1.0, v15
	v_mul_f32_e32 v84, v28, v14
	v_rcp_f32_e32 v15, v15
	v_add_f32_e32 v86, -1.0, v17
	v_mul_f32_e32 v87, v84, v84
	v_mov_b32_e32 v88, 0
	v_fma_f32 v86, v29, v86, 1.0
	s_nop 0
	v_permlane32_swap_b32_e32 v87, v88
	v_add_f32_e32 v88, v87, v88
	v_mul_f32_e32 v87, v86, v14
	v_mul_f32_e32 v14, v85, v87
	v_fmac_f32_e32 v44, 0xbf60028a, v15
	v_mul_f32_e32 v14, v30, v14
	v_mov_b32_e32 v15, 0
	s_nop 1
	v_permlane32_swap_b32_e32 v14, v15
	v_add_f32_e32 v14, v14, v15
	s_nop 1
	v_permlane16_swap_b32_e32 v88, v14
	v_add_f32_e32 v14, v88, v14
	v_exp_f32_e64 v88, -v44
	s_add_i32 s18, s92, 0x4080
	v_add_f32_dpp v14, v14, v14 row_ror:8 row_mask:0xf bank_mask:0xf bound_ctrl:1
	s_mov_b32 s15, s27
	s_mov_b32 s22, s26
	v_add_f32_dpp v14, v14, v14 row_ror:4 row_mask:0xf bank_mask:0xf bound_ctrl:1
	s_mov_b32 s23, s27
	s_and_b64 vcc, exec, s[8:9]
	v_add_f32_dpp v14, v14, v14 row_ror:2 row_mask:0xf bank_mask:0xf bound_ctrl:1
	s_nop 1
	v_add_f32_dpp v14, v14, v14 row_ror:1 row_mask:0xf bank_mask:0xf bound_ctrl:1
	s_nop 0
	v_readlane_b32 s14, v14, 0
	s_nop 1
	v_max_f32_e64 v15, s14, s14
	v_max_f32_e32 v15, 0x179abe15, v15
	v_rsq_f32_e32 v86, v15
	v_exp_f32_e32 v15, v44
	v_readlane_b32 s14, v14, 16
	v_mov_b32_e32 v14, v21
	v_mul_f32_e32 v86, v84, v86
	v_xor_b32_e32 v84, 0x80000000, v86
	v_pk_mul_f32 v[84:85], v[14:15], v[84:85]
	v_mul_f32_e32 v86, v17, v86
	v_mul_f32_e32 v21, s14, v83
	v_pk_mul_f32 v[86:87], v[88:89], v[86:87] op_sel_hi:[0,1]
	v_cvt_pk_bf16_f32 v14, v84, v85
	v_cvt_pk_bf16_f32 v21, v83, v21
	s_mov_b32 s14, s26
	v_cvt_pk_bf16_f32 v17, v86, v87
	ds_write_b16 v43, v14 offset:144
	ds_write_b16_d16_hi v43, v14 offset:4752
	ds_write_b16 v43, v17 offset:9360
	ds_write_b16_d16_hi v43, v17 offset:13968
	buffer_store_short v21, v62, s[12:15], s18 offen
	v_lshrrev_b32_e32 v14, 16, v21
	s_add_i32 s14, s94, 0x800
	buffer_store_short v14, v62, s[20:23], s14 offen
	s_cbranch_vccnz .LBB0_429
	v_cvt_pk_bf16_f32 v14, v82, s0
	s_mov_b32 s18, s26
	s_mov_b32 s19, s27
	buffer_store_short v14, v62, s[16:19], s14 offen
.LBB0_429:
	s_nop 0
	s_nop 0
	v_perm_b32 v82, v13, v13, v220
	v_sub_f32_e32 v14, v20, v82
	v_fma_f32 v20, v24, v14, v82
	s_and_b64 vcc, exec, s[4:5]
	v_mov_b32_e32 v83, v20
	s_cbranch_vccnz .LBB0_431
	s_nop 0
	s_nop 0
	v_perm_b32 v14, v40, v40, v220
	v_add_f32_e32 v14, v27, v14
	v_mul_f32_e32 v14, 0xbfb8aa3b, v14
	v_exp_f32_e32 v14, v14
	s_nop 0
	s_nop 0
	v_perm_b32 v17, v45, v45, v220
	v_add_f32_e32 v14, 1.0, v14
	v_rcp_f32_e32 v14, v14
	v_sub_f32_e32 v17, v17, v20
	v_fma_f32 v83, v14, v17, v20
.LBB0_431:
	s_nop 0
	s_nop 0
	v_perm_b32 v14, v9, v9, v220
	s_nop 0
	s_nop 0
	v_perm_b32 v21, v11, v11, v220
	v_sub_f32_e32 v16, v16, v14
	v_fma_f32 v85, v22, v16, v14
	v_sub_f32_e32 v16, v18, v21
	s_nop 0
	s_nop 0
	v_perm_b32 v17, v41, v41, v220
	s_nop 0
	s_nop 0
	v_perm_b32 v18, v42, v42, v220
	v_add_f32_e32 v18, v26, v18
	v_mul_f32_e32 v18, 0xbfb8aa3b, v18
	v_exp_f32_e32 v18, v18
	v_add_f32_e32 v17, v25, v17
	v_mul_f32_e32 v17, 0xbfb8aa3b, v17
	v_exp_f32_e32 v17, v17
	v_add_f32_e32 v18, 1.0, v18
	v_rcp_f32_e32 v86, v18
	v_fma_f32 v16, v23, v16, v21
	v_add_f32_e32 v17, 1.0, v17
	v_mul_f32_e32 v84, v28, v16
	v_rcp_f32_e32 v17, v17
	v_add_f32_e32 v18, -1.0, v86
	v_mul_f32_e32 v87, v84, v84
	v_mov_b32_e32 v88, 0
	v_fma_f32 v18, v29, v18, 1.0
	s_nop 0
	v_permlane32_swap_b32_e32 v87, v88
	v_add_f32_e32 v88, v87, v88
	v_mul_f32_e32 v87, v18, v16
	v_mul_f32_e32 v16, v85, v87
	v_fmac_f32_e32 v44, 0xbf60028a, v17
	v_mul_f32_e32 v16, v30, v16
	v_mov_b32_e32 v17, 0
	s_nop 1
	v_permlane32_swap_b32_e32 v16, v17
	v_add_f32_e32 v16, v16, v17
	s_nop 1
	v_permlane16_swap_b32_e32 v88, v16
	v_add_f32_e32 v16, v88, v16
	v_exp_f32_e64 v18, -v44
	s_add_i32 s18, s92, 0x4100
	v_add_f32_dpp v16, v16, v16 row_ror:8 row_mask:0xf bank_mask:0xf bound_ctrl:1
	s_mov_b32 s15, s27
	s_mov_b32 s22, s26
	v_add_f32_dpp v16, v16, v16 row_ror:4 row_mask:0xf bank_mask:0xf bound_ctrl:1
	s_mov_b32 s23, s27
	s_and_b64 vcc, exec, s[8:9]
	v_add_f32_dpp v16, v16, v16 row_ror:2 row_mask:0xf bank_mask:0xf bound_ctrl:1
	s_nop 1
	v_add_f32_dpp v16, v16, v16 row_ror:1 row_mask:0xf bank_mask:0xf bound_ctrl:1
	s_nop 0
	v_readlane_b32 s14, v16, 0
	s_nop 1
	v_max_f32_e64 v17, s14, s14
	v_max_f32_e32 v17, 0x179abe15, v17
	v_rsq_f32_e32 v88, v17
	v_exp_f32_e32 v17, v44
	v_readlane_b32 s14, v16, 16
	v_mov_b32_e32 v16, v15
	v_mul_f32_e32 v88, v84, v88
	v_xor_b32_e32 v84, 0x80000000, v88
	v_mul_f32_e32 v86, v86, v88
	v_pk_mul_f32 v[84:85], v[16:17], v[84:85]
	s_waitcnt vmcnt(23)
	v_pk_mul_f32 v[86:87], v[18:19], v[86:87] op_sel_hi:[0,1]
	v_mul_f32_e32 v18, s14, v83
	v_cvt_pk_bf16_f32 v15, v84, v85
	v_cvt_pk_bf16_f32 v18, v83, v18
	s_mov_b32 s14, s26
	v_cvt_pk_bf16_f32 v16, v86, v87
	ds_write_b16 v43, v15 offset:288
	ds_write_b16_d16_hi v43, v15 offset:4896
	ds_write_b16 v43, v16 offset:9504
	ds_write_b16_d16_hi v43, v16 offset:14112
	buffer_store_short v18, v62, s[12:15], s18 offen
	v_lshrrev_b32_e32 v15, 16, v18
	s_add_i32 s14, s94, 0x1000
	buffer_store_short v15, v62, s[20:23], s14 offen
	s_cbranch_vccnz .LBB0_433
	v_cvt_pk_bf16_f32 v15, v20, s0
	s_mov_b32 s18, s26
	s_mov_b32 s19, s27
	buffer_store_short v15, v62, s[16:19], s14 offen
.LBB0_433:
	s_nop 0
	s_nop 0
	v_perm_b32 v20, v12, v12, v220
	v_sub_f32_e32 v15, v82, v20
	v_fma_f32 v82, v24, v15, v20
	s_and_b64 vcc, exec, s[4:5]
	v_mov_b32_e32 v83, v82
	s_cbranch_vccnz .LBB0_435
	s_nop 0
	s_nop 0
	v_perm_b32 v15, v49, v49, v220
	v_add_f32_e32 v15, v27, v15
	v_mul_f32_e32 v15, 0xbfb8aa3b, v15
	v_exp_f32_e32 v15, v15
	s_nop 0
	s_nop 0
	v_perm_b32 v16, v47, v47, v220
	v_add_f32_e32 v15, 1.0, v15
	v_rcp_f32_e32 v15, v15
	v_sub_f32_e32 v16, v16, v82
	v_fma_f32 v83, v15, v16, v82
.LBB0_435:
	s_nop 0
	s_nop 0
	v_perm_b32 v16, v8, v8, v220
	s_nop 0
	s_nop 0
	v_perm_b32 v18, v10, v10, v220
	v_sub_f32_e32 v14, v14, v16
	v_fma_f32 v85, v22, v14, v16
	v_sub_f32_e32 v14, v21, v18
	s_nop 0
	s_nop 0
	v_perm_b32 v15, v46, v46, v220
	s_nop 0
	s_nop 0
	v_perm_b32 v21, v48, v48, v220
	v_add_f32_e32 v21, v26, v21
	v_mul_f32_e32 v21, 0xbfb8aa3b, v21
	v_exp_f32_e32 v21, v21
	v_add_f32_e32 v15, v25, v15
	v_mul_f32_e32 v15, 0xbfb8aa3b, v15
	v_exp_f32_e32 v15, v15
	v_add_f32_e32 v21, 1.0, v21
	v_rcp_f32_e32 v21, v21
	v_fma_f32 v14, v23, v14, v18
	v_add_f32_e32 v15, 1.0, v15
	v_mul_f32_e32 v84, v28, v14
	v_rcp_f32_e32 v15, v15
	v_add_f32_e32 v86, -1.0, v21
	v_mul_f32_e32 v87, v84, v84
	v_mov_b32_e32 v88, 0
	v_fma_f32 v86, v29, v86, 1.0
	s_nop 0
	v_permlane32_swap_b32_e32 v87, v88
	v_add_f32_e32 v88, v87, v88
	v_mul_f32_e32 v87, v86, v14
	v_mul_f32_e32 v14, v85, v87
	v_fmac_f32_e32 v44, 0xbf60028a, v15
	v_mul_f32_e32 v14, v30, v14
	v_mov_b32_e32 v15, 0
	s_nop 1
	v_permlane32_swap_b32_e32 v14, v15
	v_add_f32_e32 v14, v14, v15
	s_nop 1
	v_permlane16_swap_b32_e32 v88, v14
	v_add_f32_e32 v14, v88, v14
	v_exp_f32_e64 v88, -v44
	s_add_i32 s18, s92, 0x4180
	v_add_f32_dpp v14, v14, v14 row_ror:8 row_mask:0xf bank_mask:0xf bound_ctrl:1
	s_mov_b32 s15, s27
	s_mov_b32 s22, s26
	v_add_f32_dpp v14, v14, v14 row_ror:4 row_mask:0xf bank_mask:0xf bound_ctrl:1
	s_mov_b32 s23, s27
	s_and_b64 vcc, exec, s[8:9]
	v_add_f32_dpp v14, v14, v14 row_ror:2 row_mask:0xf bank_mask:0xf bound_ctrl:1
	s_nop 1
	v_add_f32_dpp v14, v14, v14 row_ror:1 row_mask:0xf bank_mask:0xf bound_ctrl:1
	s_nop 0
	v_readlane_b32 s14, v14, 0
	s_nop 1
	v_max_f32_e64 v15, s14, s14
	v_max_f32_e32 v15, 0x179abe15, v15
	v_rsq_f32_e32 v86, v15
	v_exp_f32_e32 v15, v44
	v_readlane_b32 s14, v14, 16
	v_mov_b32_e32 v14, v17
	v_mul_f32_e32 v86, v84, v86
	v_xor_b32_e32 v84, 0x80000000, v86
	v_pk_mul_f32 v[84:85], v[14:15], v[84:85]
	v_mul_f32_e32 v86, v21, v86
	v_mul_f32_e32 v21, s14, v83
	v_pk_mul_f32 v[86:87], v[88:89], v[86:87] op_sel_hi:[0,1]
	v_cvt_pk_bf16_f32 v14, v84, v85
	v_cvt_pk_bf16_f32 v21, v83, v21
	s_mov_b32 s14, s26
	v_cvt_pk_bf16_f32 v17, v86, v87
	ds_write_b16 v43, v14 offset:432
	ds_write_b16_d16_hi v43, v14 offset:5040
	ds_write_b16 v43, v17 offset:9648
	ds_write_b16_d16_hi v43, v17 offset:14256
	buffer_store_short v21, v62, s[12:15], s18 offen
	v_lshrrev_b32_e32 v14, 16, v21
	s_add_i32 s14, s94, 0x1800
	buffer_store_short v14, v62, s[20:23], s14 offen
	s_cbranch_vccz .LBB0_437
	s_cmpk_lg_i32 s2, 0xc00
	s_cbranch_scc1 .LBB0_438
	s_branch .LBB0_446

.LBB0_446:
	s_waitcnt vmcnt(24)
	s_nop 0
	s_nop 0
	v_perm_b32 v21, v79, v79, v220
	v_sub_f32_e32 v14, v20, v21
	v_fma_f32 v20, v24, v14, v21
	s_and_b64 vcc, exec, s[4:5]
	v_mov_b32_e32 v79, v20
	s_cbranch_vccnz .LBB0_448
	s_nop 0
	s_nop 0
	v_perm_b32 v14, v80, v80, v220
	v_add_f32_e32 v14, v27, v14
	v_mul_f32_e32 v14, 0xbfb8aa3b, v14
	v_exp_f32_e32 v14, v14
	s_waitcnt vmcnt(23)
	s_nop 0
	s_nop 0
	v_perm_b32 v17, v81, v81, v220
	v_add_f32_e32 v14, 1.0, v14
	v_rcp_f32_e32 v14, v14
	v_sub_f32_e32 v17, v17, v20
	v_fma_f32 v79, v17, v14, v20
.LBB0_448:
	s_nop 0
	s_nop 0
	v_perm_b32 v14, v19, v19, v220
	s_nop 0
	s_nop 0
	v_perm_b32 v17, v76, v76, v220
	v_sub_f32_e32 v16, v16, v14
	s_waitcnt vmcnt(23)
	v_fma_f32 v81, v22, v16, v14
	v_sub_f32_e32 v16, v18, v17
	s_nop 0
	s_nop 0
	v_perm_b32 v18, v77, v77, v220
	s_nop 0
	s_nop 0
	v_perm_b32 v19, v78, v78, v220
	v_add_f32_e32 v19, v26, v19
	v_mul_f32_e32 v19, 0xbfb8aa3b, v19
	v_exp_f32_e32 v19, v19
	v_add_f32_e32 v18, v25, v18
	v_mul_f32_e32 v18, 0xbfb8aa3b, v18
	v_exp_f32_e32 v18, v18
	v_add_f32_e32 v19, 1.0, v19
	v_rcp_f32_e32 v76, v19
	v_fma_f32 v16, v23, v16, v17
	v_add_f32_e32 v18, 1.0, v18
	v_mul_f32_e32 v78, v28, v16
	v_rcp_f32_e32 v18, v18
	v_add_f32_e32 v19, -1.0, v76
	v_mul_f32_e32 v77, v78, v78
	v_mov_b32_e32 v80, 0
	v_fma_f32 v19, v29, v19, 1.0
	s_nop 0
	v_permlane32_swap_b32_e32 v77, v80
	v_add_f32_e32 v80, v77, v80
	v_mul_f32_e32 v77, v16, v19
	v_mul_f32_e32 v16, v81, v77
	v_fmac_f32_e32 v44, 0xbf60028a, v18
	v_mul_f32_e32 v16, v30, v16
	v_mov_b32_e32 v18, 0
	s_nop 1
	v_permlane32_swap_b32_e32 v16, v18
	v_add_f32_e32 v16, v16, v18
	s_nop 1
	v_permlane16_swap_b32_e32 v80, v16
	v_add_f32_e32 v16, v80, v16
	v_exp_f32_e32 v19, v44
	s_add_i32 s18, s92, 0x4200
	v_add_f32_dpp v16, v16, v16 row_ror:8 row_mask:0xf bank_mask:0xf bound_ctrl:1
	s_mov_b32 s15, s27
	s_mov_b32 s22, s26
	v_add_f32_dpp v16, v16, v16 row_ror:4 row_mask:0xf bank_mask:0xf bound_ctrl:1
	s_mov_b32 s23, s27
	s_and_b64 vcc, exec, s[8:9]
	v_add_f32_dpp v16, v16, v16 row_ror:2 row_mask:0xf bank_mask:0xf bound_ctrl:1
	s_nop 1
	v_add_f32_dpp v18, v16, v16 row_ror:1 row_mask:0xf bank_mask:0xf bound_ctrl:1
	s_nop 0
	v_readlane_b32 s14, v18, 0
	s_nop 1
	v_max_f32_e64 v16, s14, s14
	v_max_f32_e32 v16, 0x179abe15, v16
	v_rsq_f32_e32 v80, v16
	v_exp_f32_e64 v16, -v44
	v_readlane_b32 s14, v18, 16
	v_mul_f32_e32 v78, v78, v80
	v_xor_b32_e32 v18, 0x80000000, v78
	v_mov_b32_e32 v80, v15
	v_pk_mul_f32 v[80:81], v[80:81], v[18:19]
	v_mul_f32_e32 v76, v76, v78
	v_mul_f32_e32 v18, s14, v79
	v_pk_mul_f32 v[76:77], v[16:17], v[76:77] op_sel_hi:[0,1]
	v_cvt_pk_bf16_f32 v15, v80, v81
	v_cvt_pk_bf16_f32 v18, v79, v18
	v_cvt_pk_bf16_f32 v16, v76, v77
	ds_write_b16 v43, v15 offset:576
	ds_write_b16_d16_hi v43, v15 offset:5184
	ds_write_b16 v43, v16 offset:9792
	ds_write_b16_d16_hi v43, v16 offset:14400
	s_mov_b32 s14, s26
	v_lshrrev_b32_e32 v15, 16, v18
	buffer_store_short v18, v62, s[12:15], s18 offen
	buffer_store_short v15, v62, s[20:23], s89 offen
	s_cbranch_vccnz .LBB0_450
	v_cvt_pk_bf16_f32 v15, v20, s0
	s_mov_b32 s18, s26
	s_mov_b32 s19, s27
	buffer_store_short v15, v62, s[16:19], s89 offen
.LBB0_450:
	s_waitcnt vmcnt(21)
	s_nop 0
	s_nop 0
	v_perm_b32 v18, v73, v73, v220
	v_sub_f32_e32 v15, v21, v18
	v_fma_f32 v21, v24, v15, v18
	s_and_b64 vcc, exec, s[4:5]
	v_mov_b32_e32 v73, v21
	s_cbranch_vccnz .LBB0_452
	s_nop 0
	s_nop 0
	v_perm_b32 v15, v74, v74, v220
	v_add_f32_e32 v15, v27, v15
	v_mul_f32_e32 v15, 0xbfb8aa3b, v15
	v_exp_f32_e32 v15, v15
	s_waitcnt vmcnt(20)
	s_nop 0
	s_nop 0
	v_perm_b32 v16, v75, v75, v220
	v_add_f32_e32 v15, 1.0, v15
	v_rcp_f32_e32 v15, v15
	v_sub_f32_e32 v16, v16, v21
	v_fma_f32 v73, v16, v15, v21
.LBB0_452:
	s_nop 0
	s_nop 0
	v_perm_b32 v15, v69, v69, v220
	s_nop 0
	s_nop 0
	v_perm_b32 v20, v70, v70, v220
	v_sub_f32_e32 v14, v14, v15
	s_waitcnt vmcnt(20)
	v_fma_f32 v75, v22, v14, v15
	v_sub_f32_e32 v14, v17, v20
	s_nop 0
	s_nop 0
	v_perm_b32 v16, v71, v71, v220
	s_nop 0
	s_nop 0
	v_perm_b32 v17, v72, v72, v220
	v_add_f32_e32 v17, v26, v17
	v_mul_f32_e32 v17, 0xbfb8aa3b, v17
	v_exp_f32_e32 v17, v17
	v_add_f32_e32 v16, v25, v16
	v_mul_f32_e32 v16, 0xbfb8aa3b, v16
	v_exp_f32_e32 v16, v16
	v_add_f32_e32 v17, 1.0, v17
	v_rcp_f32_e32 v69, v17
	v_fma_f32 v14, v23, v14, v20
	v_add_f32_e32 v16, 1.0, v16
	v_mul_f32_e32 v70, v28, v14
	v_rcp_f32_e32 v16, v16
	v_add_f32_e32 v17, -1.0, v69
	v_mul_f32_e32 v71, v70, v70
	v_mov_b32_e32 v72, 0
	v_fma_f32 v17, v29, v17, 1.0
	s_nop 0
	v_permlane32_swap_b32_e32 v71, v72
	v_add_f32_e32 v72, v71, v72
	v_mul_f32_e32 v71, v14, v17
	v_mul_f32_e32 v14, v75, v71
	v_fmac_f32_e32 v44, 0xbf60028a, v16
	v_mul_f32_e32 v14, v30, v14
	v_mov_b32_e32 v16, 0
	s_nop 1
	v_permlane32_swap_b32_e32 v14, v16
	v_add_f32_e32 v14, v14, v16
	s_nop 1
	v_permlane16_swap_b32_e32 v72, v14
	v_add_f32_e32 v14, v72, v14
	v_exp_f32_e32 v17, v44
	v_mov_b32_e32 v74, v19
	v_add_f32_dpp v14, v14, v14 row_ror:8 row_mask:0xf bank_mask:0xf bound_ctrl:1
	s_add_i32 s18, s92, 0x4280
	s_mov_b32 s15, s27
	v_add_f32_dpp v14, v14, v14 row_ror:4 row_mask:0xf bank_mask:0xf bound_ctrl:1
	s_mov_b32 s22, s26
	s_mov_b32 s23, s27
	v_add_f32_dpp v14, v14, v14 row_ror:2 row_mask:0xf bank_mask:0xf bound_ctrl:1
	s_and_b64 vcc, exec, s[8:9]
	s_nop 0
	v_add_f32_dpp v16, v14, v14 row_ror:1 row_mask:0xf bank_mask:0xf bound_ctrl:1
	s_nop 0
	v_readlane_b32 s14, v16, 0
	s_nop 1
	v_max_f32_e64 v14, s14, s14
	v_max_f32_e32 v14, 0x179abe15, v14
	v_rsq_f32_e32 v72, v14
	v_exp_f32_e64 v14, -v44
	v_readlane_b32 s14, v16, 16
	v_mul_f32_e32 v70, v70, v72
	v_xor_b32_e32 v16, 0x80000000, v70
	v_pk_mul_f32 v[74:75], v[74:75], v[16:17]
	v_mul_f32_e32 v70, v69, v70
	v_mul_f32_e32 v19, s14, v73
	v_pk_mul_f32 v[70:71], v[14:15], v[70:71] op_sel_hi:[0,1]
	v_cvt_pk_bf16_f32 v14, v74, v75
	v_cvt_pk_bf16_f32 v19, v73, v19
	v_cvt_pk_bf16_f32 v16, v70, v71
	ds_write_b16 v43, v14 offset:720
	ds_write_b16_d16_hi v43, v14 offset:5328
	ds_write_b16 v43, v16 offset:9936
	ds_write_b16_d16_hi v43, v16 offset:14544
	s_mov_b32 s14, s26
	v_lshrrev_b32_e32 v14, 16, v19
	buffer_store_short v19, v62, s[12:15], s18 offen
	buffer_store_short v14, v62, s[20:23], s88 offen
	s_cbranch_vccnz .LBB0_454
	v_cvt_pk_bf16_f32 v14, v21, s0
	s_mov_b32 s18, s26
	s_mov_b32 s19, s27
	buffer_store_short v14, v62, s[16:19], s88 offen
.LBB0_454:
	s_waitcnt vmcnt(18)
	s_nop 0
	s_nop 0
	v_perm_b32 v19, v63, v63, v220
	v_sub_f32_e32 v14, v18, v19
	v_fma_f32 v21, v24, v14, v19
	s_and_b64 vcc, exec, s[4:5]
	v_mov_b32_e32 v63, v21
	s_cbranch_vccnz .LBB0_456
	s_nop 0
	s_nop 0
	v_perm_b32 v14, v57, v57, v220
	v_add_f32_e32 v14, v27, v14
	v_mul_f32_e32 v14, 0xbfb8aa3b, v14
	v_exp_f32_e32 v14, v14
	s_waitcnt vmcnt(17)
	s_nop 0
	s_nop 0
	v_perm_b32 v16, v68, v68, v220
	v_add_f32_e32 v14, 1.0, v14
	v_rcp_f32_e32 v14, v14
	v_sub_f32_e32 v16, v16, v21
	v_fma_f32 v63, v16, v14, v21
.LBB0_456:
	s_nop 0
	s_nop 0
	v_perm_b32 v16, v58, v58, v220
	s_nop 0
	s_nop 0
	v_perm_b32 v18, v59, v59, v220
	v_sub_f32_e32 v14, v15, v16
	v_fma_f32 v59, v22, v14, v16
	v_sub_f32_e32 v14, v20, v18
	s_nop 0
	s_nop 0
	v_perm_b32 v15, v60, v60, v220
	s_waitcnt vmcnt(17)
	s_nop 0
	s_nop 0
	v_perm_b32 v20, v61, v61, v220
	v_add_f32_e32 v20, v26, v20
	v_mul_f32_e32 v20, 0xbfb8aa3b, v20
	v_exp_f32_e32 v20, v20
	v_add_f32_e32 v15, v25, v15
	v_mul_f32_e32 v15, 0xbfb8aa3b, v15
	v_exp_f32_e32 v15, v15
	v_add_f32_e32 v20, 1.0, v20
	v_rcp_f32_e32 v57, v20
	v_fma_f32 v14, v23, v14, v18
	v_add_f32_e32 v15, 1.0, v15
	v_mul_f32_e32 v58, v28, v14
	v_rcp_f32_e32 v15, v15
	v_add_f32_e32 v20, -1.0, v57
	v_mul_f32_e32 v60, v58, v58
	v_mov_b32_e32 v61, 0
	v_fma_f32 v20, v29, v20, 1.0
	s_nop 0
	v_permlane32_swap_b32_e32 v60, v61
	v_add_f32_e32 v60, v60, v61
	v_mul_f32_e32 v61, v14, v20
	v_mul_f32_e32 v14, v59, v61
	v_fmac_f32_e32 v44, 0xbf60028a, v15
	v_mul_f32_e32 v14, v30, v14
	v_mov_b32_e32 v15, 0
	s_nop 1
	v_permlane32_swap_b32_e32 v14, v15
	v_add_f32_e32 v14, v14, v15
	s_nop 1
	v_permlane16_swap_b32_e32 v60, v14
	v_add_f32_e32 v14, v60, v14
	v_exp_f32_e64 v20, -v44
	s_add_i32 s18, s92, 0x4300
	v_add_f32_dpp v14, v14, v14 row_ror:8 row_mask:0xf bank_mask:0xf bound_ctrl:1
	s_mov_b32 s15, s27
	s_mov_b32 s22, s26
	v_add_f32_dpp v14, v14, v14 row_ror:4 row_mask:0xf bank_mask:0xf bound_ctrl:1
	s_mov_b32 s23, s27
	s_and_b64 vcc, exec, s[8:9]
	v_add_f32_dpp v14, v14, v14 row_ror:2 row_mask:0xf bank_mask:0xf bound_ctrl:1
	s_nop 1
	v_add_f32_dpp v14, v14, v14 row_ror:1 row_mask:0xf bank_mask:0xf bound_ctrl:1
	s_nop 0
	v_readlane_b32 s14, v14, 0
	s_nop 1
	v_max_f32_e64 v15, s14, s14
	v_max_f32_e32 v15, 0x179abe15, v15
	v_rsq_f32_e32 v60, v15
	v_exp_f32_e32 v15, v44
	v_readlane_b32 s14, v14, 16
	v_mul_f32_e32 v60, v58, v60
	v_xor_b32_e32 v14, 0x80000000, v60
	v_mov_b32_e32 v58, v17
	v_mul_f32_e32 v60, v57, v60
	v_pk_mul_f32 v[58:59], v[58:59], v[14:15]
	v_pk_mul_f32 v[60:61], v[20:21], v[60:61] op_sel_hi:[0,1]
	v_mul_f32_e32 v20, s14, v63
	v_cvt_pk_bf16_f32 v14, v58, v59
	v_cvt_pk_bf16_f32 v20, v63, v20
	v_cvt_pk_bf16_f32 v17, v60, v61
	ds_write_b16 v43, v14 offset:864
	ds_write_b16_d16_hi v43, v14 offset:5472
	ds_write_b16 v43, v17 offset:10080
	ds_write_b16_d16_hi v43, v17 offset:14688
	s_mov_b32 s14, s26
	v_lshrrev_b32_e32 v14, 16, v20
	buffer_store_short v20, v62, s[12:15], s18 offen
	buffer_store_short v14, v62, s[20:23], s87 offen
	s_cbranch_vccnz .LBB0_458
	v_cvt_pk_bf16_f32 v14, v21, s0
	s_mov_b32 s18, s26
	s_mov_b32 s19, s27
	buffer_store_short v14, v62, s[16:19], s87 offen
.LBB0_458:
	s_waitcnt vmcnt(15)
	s_nop 0
	s_nop 0
	v_perm_b32 v14, v52, v52, v220
	v_sub_f32_e32 v17, v19, v14
	v_fmac_f32_e32 v14, v24, v17
	s_and_b64 vcc, exec, s[4:5]
	v_mov_b32_e32 v17, v14
	s_cbranch_vccnz .LBB0_460
	s_nop 0
	s_nop 0
	v_perm_b32 v17, v55, v55, v220
	v_add_f32_e32 v17, v27, v17
	v_mul_f32_e32 v17, 0xbfb8aa3b, v17
	v_exp_f32_e32 v17, v17
	s_waitcnt vmcnt(14)
	s_nop 0
	s_nop 0
	v_perm_b32 v19, v56, v56, v220
	v_add_f32_e32 v17, 1.0, v17
	v_rcp_f32_e32 v17, v17
	v_sub_f32_e32 v19, v19, v14
	v_fma_f32 v17, v19, v17, v14
.LBB0_460:
	s_nop 0
	s_nop 0
	v_perm_b32 v19, v50, v50, v220
	s_nop 0
	s_nop 0
	v_perm_b32 v20, v51, v51, v220
	v_sub_f32_e32 v16, v16, v19
	v_fmac_f32_e32 v19, v22, v16
	v_sub_f32_e32 v16, v18, v20
	s_nop 0
	s_nop 0
	v_perm_b32 v18, v53, v53, v220
	s_waitcnt vmcnt(14)
	s_nop 0
	s_nop 0
	v_perm_b32 v21, v54, v54, v220
	v_add_f32_e32 v21, v26, v21
	v_mul_f32_e32 v21, 0xbfb8aa3b, v21
	v_exp_f32_e32 v21, v21
	v_add_f32_e32 v18, v25, v18
	v_mul_f32_e32 v18, 0xbfb8aa3b, v18
	v_exp_f32_e32 v18, v18
	v_fmac_f32_e32 v20, v23, v16
	v_add_f32_e32 v16, 1.0, v21
	v_rcp_f32_e32 v21, v16
	v_add_f32_e32 v16, 1.0, v18
	v_rcp_f32_e32 v16, v16
	v_mul_f32_e32 v18, v28, v20
	v_add_f32_e32 v53, -1.0, v21
	v_mul_f32_e32 v54, v18, v18
	v_mov_b32_e32 v55, 0
	v_fma_f32 v53, v29, v53, 1.0
	s_nop 0
	v_permlane32_swap_b32_e32 v54, v55
	v_add_f32_e32 v54, v54, v55
	v_mul_f32_e32 v55, v20, v53
	v_fmac_f32_e32 v44, 0xbf60028a, v16
	v_mul_f32_e32 v16, v19, v55
	v_mul_f32_e32 v16, v30, v16
	v_mov_b32_e32 v20, 0
	s_nop 1
	v_permlane32_swap_b32_e32 v16, v20
	v_add_f32_e32 v16, v16, v20
	s_nop 1
	v_permlane16_swap_b32_e32 v54, v16
	v_add_f32_e32 v16, v54, v16
	v_exp_f32_e32 v20, v44
	s_addk_i32 s92, 0x4380
	v_add_f32_dpp v16, v16, v16 row_ror:8 row_mask:0xf bank_mask:0xf bound_ctrl:1
	s_mov_b32 s15, s27
	v_mov_b32_e32 v57, v20
	v_add_f32_dpp v16, v16, v16 row_ror:4 row_mask:0xf bank_mask:0xf bound_ctrl:1
	s_mov_b32 s22, s26
	s_mov_b32 s23, s27
	v_add_f32_dpp v16, v16, v16 row_ror:2 row_mask:0xf bank_mask:0xf bound_ctrl:1
	s_and_b64 vcc, exec, s[8:9]
	s_nop 0
	v_add_f32_dpp v53, v16, v16 row_ror:1 row_mask:0xf bank_mask:0xf bound_ctrl:1
	s_nop 0
	v_readlane_b32 s14, v53, 0
	s_nop 1
	v_max_f32_e64 v16, s14, s14
	v_max_f32_e32 v16, 0x179abe15, v16
	v_rsq_f32_e32 v54, v16
	v_exp_f32_e64 v16, -v44
	v_readlane_b32 s14, v53, 16
	v_mul_f32_e32 v53, v18, v54
	v_xor_b32_e32 v56, 0x80000000, v53
	v_mov_b32_e32 v18, v15
	v_pk_mul_f32 v[18:19], v[18:19], v[56:57]
	v_mul_f32_e32 v54, v21, v53
	v_cvt_pk_bf16_f32 v15, v18, v19
	v_mul_f32_e32 v18, s14, v17
	v_pk_mul_f32 v[54:55], v[16:17], v[54:55] op_sel_hi:[0,1]
	v_cvt_pk_bf16_f32 v17, v17, v18
	v_cvt_pk_bf16_f32 v16, v54, v55
	ds_write_b16 v43, v15 offset:1008
	ds_write_b16_d16_hi v43, v15 offset:5616
	ds_write_b16 v43, v16 offset:10224
	ds_write_b16_d16_hi v43, v16 offset:14832
	s_mov_b32 s14, s26
	v_lshrrev_b32_e32 v15, 16, v17
	buffer_store_short v17, v62, s[12:15], s92 offen
	buffer_store_short v15, v62, s[20:23], s86 offen
	s_cbranch_vccnz .LBB0_462
	v_cvt_pk_bf16_f32 v14, v14, s0
	s_mov_b32 s18, s26
	s_mov_b32 s19, s27
	buffer_store_short v14, v62, s[16:19], s86 offen
